# baseline (speedup 1.0000x reference)
.Lpoll_l_g2:
	s_sleep 2
	global_load_dword v254, v[252:253], off sc1
	s_cmp_gt_u32 s14, 0xffffd
	s_cselect_b64 s[12:13], -1, 0
	s_add_i32 s14, s14, 1
	s_waitcnt vmcnt(0)
	v_cmp_lt_i32_e64 s[16:17], 3, v254
	s_or_b64 s[12:13], s[16:17], s[12:13]
	s_and_b64 s[12:13], exec, s[12:13]
	s_or_b64 s[10:11], s[12:13], s[10:11]
	s_andn2_b64 exec, exec, s[10:11]
	s_cbranch_execnz .Lpoll_l_g2
